# passCU: node tiles of 25 nodes (4000 active waves instead of 3125), padded rows masked out of y1 stores and BN statistics
# speedup vs baseline: 1.1230x; 1.0301x over previous
_Z8k_passCUILi1EEvPKiS1_PKfPKtS5_S3_S3_S3_S3_S3_S3_PK15HIP_vector_typeIjLj4EES9_S9_PKdSB_S1_S1_S5_S3_PtPd:
	s_load_dwordx4 s[4:7], s[0:1], 0x58
	s_load_dwordx2 s[8:9], s[0:1], 0x68
	s_load_dword s50, s[0:1], 0xb0
	s_load_dwordx2 s[52:53], s[0:1], 0x80
	s_load_dwordx4 s[56:59], s[0:1], 0x0
	s_load_dwordx2 s[60:61], s[0:1], 0x10
	v_mov_b32_e32 v3, 0
	v_lshlrev_b32_e32 v2, 4, v0
	s_movk_i32 s3, 0x2000
	s_waitcnt lgkmcnt(0)
	v_readfirstlane_b32 s54, v0
	v_lshrrev_b32_e32 v82, 3, v0
	v_and_b32_e32 v82, 7, v82
	v_lshlrev_b32_e32 v82, 4, v82
	s_lshr_b32 s54, s54, 6
	s_mul_i32 s55, s50, s54
	s_add_i32 s55, s55, s2
	s_min_u32 s55, s55, 0xf9f
	s_mul_i32 s55, s55, 100
	s_add_u32 s52, s52, s55
	s_addc_u32 s53, s53, 0
	s_load_dword s62, s[52:53], 0x0
	s_load_dword s64, s[52:53], 0x64
	v_lshl_add_u64 v[16:17], s[6:7], 0, v[2:3]
	global_load_dwordx4 v[4:7], v2, s[4:5]
	global_load_dwordx4 v[8:11], v2, s[6:7]
	global_load_dwordx4 v[12:15], v2, s[8:9]
	v_add_co_u32_e32 v16, vcc, s3, v16
	v_lshl_add_u64 v[20:21], s[8:9], 0, v[2:3]
	s_nop 0
	v_addc_co_u32_e32 v17, vcc, 0, v17, vcc
	v_add_co_u32_e32 v20, vcc, 0x2000, v20
	global_load_dwordx4 v[16:19], v[16:17], off
	s_nop 0
	v_addc_co_u32_e32 v21, vcc, 0, v21, vcc
	global_load_dwordx4 v[20:23], v[20:21], off
	s_mov_b32 s28, 0
	v_readfirstlane_b32 s3, v0
	v_cmp_gt_u32_e32 vcc, 64, v0
	s_waitcnt vmcnt(4)
	ds_write_b128 v2, v[4:7]
	s_waitcnt vmcnt(3)
	ds_write_b128 v2, v[8:11] offset:16384
	s_waitcnt vmcnt(2)
	ds_write_b128 v2, v[12:15] offset:32768
	s_waitcnt vmcnt(1)
	ds_write_b128 v2, v[16:19] offset:24576
	s_waitcnt vmcnt(0)
	ds_write_b128 v2, v[20:23] offset:40960
	s_waitcnt lgkmcnt(0)
	s_lshl_b32 s63, s62, 2
	v_add_u32_e32 v83, s63, v82
	global_load_dwordx4 v[70:73], v83, s[56:57]
	global_load_dwordx4 v[74:77], v83, s[58:59]
	global_load_dwordx4 v[78:81], v83, s[60:61]
	s_and_saveexec_b64 s[20:21], vcc
	s_cbranch_execz .LBB8_2
	s_load_dwordx4 s[4:7], s[0:1], 0x70
	s_load_dwordx4 s[16:19], s[0:1], 0x48
	v_lshlrev_b32_e32 v2, 3, v0
	s_load_dwordx8 s[8:15], s[0:1], 0x28
	v_lshlrev_b32_e32 v1, 2, v0
	s_waitcnt lgkmcnt(0)
	global_load_dwordx2 v[4:5], v2, s[4:5]
	global_load_dwordx2 v[6:7], v2, s[4:5] offset:512
	global_load_dwordx2 v[8:9], v2, s[4:5] offset:1024
	global_load_dwordx2 v[10:11], v2, s[4:5] offset:1536
	global_load_dwordx2 v[12:13], v2, s[4:5] offset:2048
	global_load_dwordx2 v[14:15], v2, s[4:5] offset:2560
	global_load_dwordx2 v[16:17], v2, s[4:5] offset:3072
	global_load_dwordx2 v[18:19], v2, s[4:5] offset:3584
	v_lshl_add_u64 v[20:21], s[4:5], 0, v[2:3]
	s_movk_i32 s4, 0x1000
	v_add_co_u32_e32 v36, vcc, s4, v20
	s_mov_b32 s24, 0
	s_nop 0
	v_addc_co_u32_e32 v37, vcc, 0, v21, vcc
	global_load_dwordx2 v[20:21], v[36:37], off
	global_load_dwordx2 v[22:23], v[36:37], off offset:512
	global_load_dwordx2 v[24:25], v[36:37], off offset:1024
	global_load_dwordx2 v[26:27], v[36:37], off offset:1536
	global_load_dwordx2 v[28:29], v[36:37], off offset:2048
	global_load_dwordx2 v[30:31], v[36:37], off offset:2560
	global_load_dwordx2 v[32:33], v[36:37], off offset:3072
	global_load_dwordx2 v[34:35], v[36:37], off offset:3584
	global_load_dword v67, v1, s[10:11]
	global_load_dword v68, v1, s[12:13]
	global_load_dwordx2 v[38:39], v2, s[6:7] offset:512
	global_load_dwordx2 v[40:41], v2, s[6:7]
	global_load_dwordx2 v[42:43], v2, s[6:7] offset:1536
	global_load_dwordx2 v[44:45], v2, s[6:7] offset:1024
	global_load_dwordx2 v[46:47], v2, s[6:7] offset:2560
	global_load_dwordx2 v[48:49], v2, s[6:7] offset:2048
	global_load_dwordx2 v[50:51], v2, s[6:7] offset:3584
	global_load_dwordx2 v[52:53], v2, s[6:7] offset:3072
	v_lshl_add_u64 v[36:37], s[6:7], 0, v[2:3]
	v_add_co_u32_e32 v2, vcc, s4, v36
	s_mov_b32 s25, 0x412e8480
	s_nop 0
	v_addc_co_u32_e32 v3, vcc, 0, v37, vcc
	global_load_dwordx2 v[36:37], v[2:3], off
	global_load_dwordx2 v[54:55], v[2:3], off offset:512
	global_load_dwordx2 v[56:57], v[2:3], off offset:1024
	global_load_dwordx2 v[58:59], v[2:3], off offset:1536
	global_load_dwordx2 v[60:61], v[2:3], off offset:2048
	global_load_dwordx2 v[62:63], v[2:3], off offset:2560
	global_load_dwordx2 v[64:65], v[2:3], off offset:3072
	s_nop 0
	global_load_dwordx2 v[2:3], v[2:3], off offset:3584
	s_mov_b32 s22, 0x88e368f1
	s_mov_b32 s23, 0x3ee4f8b5
	s_mov_b32 s26, 0
	s_brev_b32 s27, 8
	v_mov_b32_e32 v66, 0x100
	s_waitcnt vmcnt(33)
	v_add_f64 v[4:5], v[4:5], 0
	s_waitcnt vmcnt(32)
	v_add_f64 v[6:7], v[6:7], 0
	s_waitcnt vmcnt(31)
	v_add_f64 v[4:5], v[4:5], v[8:9]
	s_waitcnt vmcnt(30)
	v_add_f64 v[6:7], v[6:7], v[10:11]
	s_waitcnt vmcnt(29)
	v_add_f64 v[4:5], v[4:5], v[12:13]
	s_waitcnt vmcnt(28)
	v_add_f64 v[6:7], v[6:7], v[14:15]
	s_waitcnt vmcnt(27)
	v_add_f64 v[4:5], v[4:5], v[16:17]
	s_waitcnt vmcnt(26)
	v_add_f64 v[6:7], v[6:7], v[18:19]
	s_waitcnt vmcnt(25)
	v_add_f64 v[4:5], v[4:5], v[20:21]
	s_waitcnt vmcnt(24)
	v_add_f64 v[6:7], v[6:7], v[22:23]
	s_waitcnt vmcnt(23)
	v_add_f64 v[4:5], v[4:5], v[24:25]
	s_waitcnt vmcnt(22)
	v_add_f64 v[6:7], v[6:7], v[26:27]
	s_waitcnt vmcnt(21)
	v_add_f64 v[4:5], v[4:5], v[28:29]
	s_waitcnt vmcnt(20)
	v_add_f64 v[6:7], v[6:7], v[30:31]
	s_waitcnt vmcnt(19)
	v_add_f64 v[4:5], v[4:5], v[32:33]
	s_waitcnt vmcnt(18)
	v_add_f64 v[6:7], v[6:7], v[34:35]
	v_div_scale_f64 v[8:9], s[4:5], s[24:25], s[24:25], v[4:5]
	v_div_scale_f64 v[12:13], s[4:5], s[24:25], s[24:25], v[6:7]
	v_rcp_f64_e32 v[14:15], v[8:9]
	v_rcp_f64_e32 v[16:17], v[12:13]
	v_div_scale_f64 v[10:11], vcc, v[4:5], s[24:25], v[4:5]
	v_fma_f64 v[20:21], -v[8:9], v[14:15], 1.0
	v_fma_f64 v[22:23], -v[12:13], v[16:17], 1.0
	v_fmac_f64_e32 v[14:15], v[14:15], v[20:21]
	v_fmac_f64_e32 v[16:17], v[16:17], v[22:23]
	v_fma_f64 v[20:21], -v[8:9], v[14:15], 1.0
	v_fma_f64 v[22:23], -v[12:13], v[16:17], 1.0
	v_fmac_f64_e32 v[14:15], v[14:15], v[20:21]
	v_div_scale_f64 v[18:19], s[4:5], v[6:7], s[24:25], v[6:7]
	v_fmac_f64_e32 v[16:17], v[16:17], v[22:23]
	v_mul_f64 v[20:21], v[10:11], v[14:15]
	v_mul_f64 v[22:23], v[18:19], v[16:17]
	v_fma_f64 v[8:9], -v[8:9], v[20:21], v[10:11]
	v_fma_f64 v[10:11], -v[12:13], v[22:23], v[18:19]
	v_div_fmas_f64 v[8:9], v[8:9], v[14:15], v[20:21]
	s_mov_b64 vcc, s[4:5]
	v_div_fixup_f64 v[4:5], v[8:9], s[24:25], v[4:5]
	v_div_fmas_f64 v[8:9], v[10:11], v[16:17], v[22:23]
	v_div_fixup_f64 v[6:7], v[8:9], s[24:25], v[6:7]
	v_fma_f64 v[6:7], -v[4:5], v[4:5], v[6:7]
	v_cmp_ngt_f64_e32 vcc, 0, v[6:7]
	global_load_dword v22, v1, s[8:9]
	global_load_dword v23, v1, s[14:15]
	global_load_dword v24, v1, s[16:17]
	global_load_dword v25, v1, s[18:19]
	v_cndmask_b32_e32 v7, 0, v7, vcc
	v_cndmask_b32_e32 v6, 0, v6, vcc
	v_add_f64 v[6:7], v[6:7], s[22:23]
	v_cmp_gt_f64_e32 vcc, s[26:27], v[6:7]
	v_mov_b32_e32 v26, 0xffffff80
	v_mov_b32_e32 v27, 0x260
	v_cndmask_b32_e32 v8, 0, v66, vcc
	v_ldexp_f64 v[6:7], v[6:7], v8
	v_rsq_f64_e32 v[8:9], v[6:7]
	s_waitcnt vmcnt(21)
	v_cvt_f64_f32_e32 v[10:11], v67
	v_add_f64 v[4:5], v[4:5], 0
	v_mul_f64 v[12:13], v[6:7], v[8:9]
	v_mul_f64 v[8:9], v[8:9], 0.5
	v_fma_f64 v[14:15], -v[8:9], v[12:13], 0.5
	v_fmac_f64_e32 v[12:13], v[12:13], v[14:15]
	v_fmac_f64_e32 v[8:9], v[8:9], v[14:15]
	v_fma_f64 v[14:15], -v[12:13], v[12:13], v[6:7]
	v_fmac_f64_e32 v[12:13], v[14:15], v[8:9]
	v_fma_f64 v[14:15], -v[12:13], v[12:13], v[6:7]
	v_fmac_f64_e32 v[12:13], v[14:15], v[8:9]
	v_cndmask_b32_e32 v8, 0, v26, vcc
	v_ldexp_f64 v[8:9], v[12:13], v8
	v_cmp_class_f64_e32 vcc, v[6:7], v27
	s_nop 1
	v_cndmask_b32_e32 v7, v9, v7, vcc
	v_cndmask_b32_e32 v6, v8, v6, vcc
	v_div_scale_f64 v[8:9], s[4:5], v[6:7], v[6:7], v[10:11]
	v_rcp_f64_e32 v[12:13], v[8:9]
	s_nop 0
	v_fma_f64 v[14:15], -v[8:9], v[12:13], 1.0
	v_fmac_f64_e32 v[12:13], v[12:13], v[14:15]
	v_fma_f64 v[14:15], -v[8:9], v[12:13], 1.0
	v_fmac_f64_e32 v[12:13], v[12:13], v[14:15]
	v_div_scale_f64 v[14:15], vcc, v[10:11], v[6:7], v[10:11]
	v_mul_f64 v[16:17], v[14:15], v[12:13]
	v_fma_f64 v[8:9], -v[8:9], v[16:17], v[14:15]
	s_nop 1
	v_div_fmas_f64 v[8:9], v[8:9], v[12:13], v[16:17]
	v_div_fixup_f64 v[6:7], v[8:9], v[6:7], v[10:11]
	s_waitcnt vmcnt(18)
	v_add_f64 v[10:11], v[40:41], 0
	s_waitcnt vmcnt(16)
	v_add_f64 v[10:11], v[10:11], v[44:45]
	s_waitcnt vmcnt(14)
	v_add_f64 v[10:11], v[10:11], v[48:49]
	s_waitcnt vmcnt(12)
	v_add_f64 v[10:11], v[10:11], v[52:53]
	s_waitcnt vmcnt(11)
	v_add_f64 v[10:11], v[10:11], v[36:37]
	s_waitcnt vmcnt(9)
	v_add_f64 v[10:11], v[10:11], v[56:57]
	v_add_f64 v[12:13], v[38:39], 0
	s_waitcnt vmcnt(7)
	v_add_f64 v[10:11], v[10:11], v[60:61]
	v_add_f64 v[12:13], v[12:13], v[42:43]
	s_waitcnt vmcnt(5)
	v_add_f64 v[10:11], v[10:11], v[64:65]
	v_add_f64 v[12:13], v[12:13], v[46:47]
	v_div_scale_f64 v[14:15], s[4:5], s[24:25], s[24:25], v[10:11]
	v_add_f64 v[12:13], v[12:13], v[50:51]
	v_rcp_f64_e32 v[16:17], v[14:15]
	v_add_f64 v[12:13], v[12:13], v[54:55]
	v_add_f64 v[12:13], v[12:13], v[58:59]
	v_add_f64 v[12:13], v[12:13], v[62:63]
	s_waitcnt vmcnt(4)
	v_add_f64 v[2:3], v[12:13], v[2:3]
	v_fma_f64 v[12:13], -v[14:15], v[16:17], 1.0
	v_fmac_f64_e32 v[16:17], v[16:17], v[12:13]
	v_fma_f64 v[12:13], -v[14:15], v[16:17], 1.0
	v_fmac_f64_e32 v[16:17], v[16:17], v[12:13]
	v_div_scale_f64 v[12:13], vcc, v[10:11], s[24:25], v[10:11]
	v_mul_f64 v[18:19], v[12:13], v[16:17]
	v_fma_f64 v[12:13], -v[14:15], v[18:19], v[12:13]
	v_div_scale_f64 v[14:15], s[4:5], s[24:25], s[24:25], v[2:3]
	v_rcp_f64_e32 v[20:21], v[14:15]
	v_div_fmas_f64 v[12:13], v[12:13], v[16:17], v[18:19]
	v_div_fixup_f64 v[10:11], v[12:13], s[24:25], v[10:11]
	v_cvt_f64_f32_e32 v[8:9], v68
	v_fma_f64 v[12:13], -v[14:15], v[20:21], 1.0
	v_fmac_f64_e32 v[20:21], v[20:21], v[12:13]
	v_fma_f64 v[12:13], -v[14:15], v[20:21], 1.0
	v_fmac_f64_e32 v[20:21], v[20:21], v[12:13]
	v_div_scale_f64 v[12:13], vcc, v[2:3], s[24:25], v[2:3]
	v_mul_f64 v[16:17], v[12:13], v[20:21]
	v_fma_f64 v[12:13], -v[14:15], v[16:17], v[12:13]
	v_cvt_f32_f64_e32 v28, v[6:7]
	s_nop 0
	v_div_fmas_f64 v[12:13], v[12:13], v[20:21], v[16:17]
	v_div_fixup_f64 v[2:3], v[12:13], s[24:25], v[2:3]
	v_fma_f64 v[2:3], -v[10:11], v[10:11], v[2:3]
	v_cmp_ngt_f64_e32 vcc, 0, v[2:3]
	v_fma_f64 v[4:5], -v[4:5], v[6:7], v[8:9]
	v_cvt_f32_f64_e32 v16, v[4:5]
	v_cndmask_b32_e32 v3, 0, v3, vcc
	v_cndmask_b32_e32 v2, 0, v2, vcc
	v_add_f64 v[2:3], v[2:3], s[22:23]
	v_cmp_gt_f64_e32 vcc, s[26:27], v[2:3]
	s_waitcnt vmcnt(1)
	v_cvt_f64_f32_e32 v[4:5], v24
	ds_write2st64_b32 v1, v28, v16 offset0:208 offset1:209
	v_cndmask_b32_e32 v12, 0, v66, vcc
	v_ldexp_f64 v[2:3], v[2:3], v12
	v_rsq_f64_e32 v[12:13], v[2:3]
	v_mul_f32_e32 v18, v22, v28
	v_mul_f64 v[6:7], v[2:3], v[12:13]
	v_mul_f64 v[8:9], v[12:13], 0.5
	v_fma_f64 v[12:13], -v[8:9], v[6:7], 0.5
	v_fmac_f64_e32 v[6:7], v[6:7], v[12:13]
	v_fma_f64 v[14:15], -v[6:7], v[6:7], v[2:3]
	v_fmac_f64_e32 v[8:9], v[8:9], v[12:13]
	v_fmac_f64_e32 v[6:7], v[14:15], v[8:9]
	v_fma_f64 v[12:13], -v[6:7], v[6:7], v[2:3]
	v_fmac_f64_e32 v[6:7], v[12:13], v[8:9]
	v_cndmask_b32_e32 v8, 0, v26, vcc
	v_ldexp_f64 v[6:7], v[6:7], v8
	v_cmp_class_f64_e32 vcc, v[2:3], v27
	v_cvt_f64_f32_e32 v[12:13], v23
	s_nop 0
	v_cndmask_b32_e32 v3, v7, v3, vcc
	v_cndmask_b32_e32 v2, v6, v2, vcc
	v_div_scale_f64 v[6:7], s[4:5], v[2:3], v[2:3], v[4:5]
	v_rcp_f64_e32 v[8:9], v[6:7]
	s_nop 0
	v_fma_f64 v[14:15], -v[6:7], v[8:9], 1.0
	v_fmac_f64_e32 v[8:9], v[8:9], v[14:15]
	v_fma_f64 v[14:15], -v[6:7], v[8:9], 1.0
	v_fmac_f64_e32 v[8:9], v[8:9], v[14:15]
	v_div_scale_f64 v[14:15], vcc, v[4:5], v[2:3], v[4:5]
	v_mul_f64 v[16:17], v[14:15], v[8:9]
	v_fma_f64 v[6:7], -v[6:7], v[16:17], v[14:15]
	s_nop 1
	v_div_fmas_f64 v[6:7], v[6:7], v[8:9], v[16:17]
	v_div_fixup_f64 v[2:3], v[6:7], v[2:3], v[4:5]
	s_waitcnt vmcnt(0)
	v_cvt_f64_f32_e32 v[4:5], v25
	v_add_f64 v[6:7], v[10:11], v[12:13]
	v_cvt_f32_f64_e32 v8, v[2:3]
	v_fma_f64 v[2:3], -v[6:7], v[2:3], v[4:5]
	v_cvt_f32_f64_e32 v2, v[2:3]
	v_fmac_f32_e32 v2, v23, v8
	ds_write2st64_b32 v1, v18, v8 offset0:210 offset1:211
	ds_write_b32 v1, v2 offset:54272
.LBB8_2:
	s_or_b64 exec, exec, s[20:21]
	s_waitcnt lgkmcnt(0)
	s_barrier
	s_load_dword s4, s[0:1], 0xb0
	v_and_b32_e32 v98, 31, v0
	v_lshlrev_b32_e32 v1, 3, v98
	s_lshr_b32 s3, s3, 6
	v_add_u32_e32 v1, 0xd000, v1
	ds_read2_b64 v[66:69], v1 offset0:96 offset1:128
	s_waitcnt lgkmcnt(0)
	s_mul_i32 s4, s4, s3
	s_add_i32 s4, s4, s2
	s_mul_i32 s14, s4, 25
	s_cmpk_lt_i32 s4, 0xfa0
	s_cselect_b64 s[16:17], -1, 0
	s_cmpk_gt_i32 s4, 0xf9f
	s_mov_b32 s20, 0
	s_mov_b32 s37, 0
	s_cbranch_scc1 .LBB8_4
	s_mov_b32 s20, s62
	s_mov_b32 s28, s64
.LBB8_4:
	s_load_dwordx2 s[12:13], s[0:1], 0xa8
	s_load_dwordx2 s[18:19], s[0:1], 0x98
	s_waitcnt lgkmcnt(0)
	s_sub_i32 s4, s28, s20
	s_add_i32 s4, s4, 31
	v_and_b32_e32 v1, 63, v0
	s_ashr_i32 s15, s4, 5
	s_cmp_lt_i32 s15, 1
	v_add_u32_e32 v90, s14, v98
	v_and_b32_e32 v100, 32, v0
	v_lshlrev_b32_e32 v99, 4, v1
	s_cbranch_scc1 .LBB8_7
	s_load_dwordx8 s[4:11], s[0:1], 0x0
	s_load_dwordx2 s[24:25], s[0:1], 0x20
	s_load_dwordx2 s[30:31], s[0:1], 0x80
	s_load_dwordx2 s[48:49], s[0:1], 0x90
	v_and_b32_e32 v34, 7, v1
	v_lshlrev_b32_e32 v34, 4, v34
	v_lshrrev_b32_e32 v35, 3, v1
	s_lshl_b32 s32, s3, 12
	s_add_i32 s33, s32, 0x2000
	s_add_i32 s32, s32, 0xb500
	s_cmp_lt_u32 s3, 2
	s_cselect_b32 s32, s33, s32
	v_lshlrev_b32_e32 v36, 1, v35
	v_and_b32_e32 v36, 7, v36
	v_or_b32_e32 v37, 1, v36
	v_lshlrev_b32_e32 v36, 4, v36
	v_lshlrev_b32_e32 v37, 4, v37
	v_xor_b32_e32 v36, v36, v34
	v_xor_b32_e32 v37, v37, v34
	v_lshl_add_u32 v39, v35, 9, s32
	v_add_u32_e32 v36, v36, v39
	v_add_u32_e32 v37, v37, v39
	v_lshrrev_b32_e32 v38, 1, v98
	v_and_b32_e32 v38, 7, v38
	v_lshrrev_b32_e32 v39, 3, v100
	v_xor_b32_e32 v38, v38, v39
	v_lshlrev_b32_e32 v38, 4, v38
	v_lshl_add_u32 v39, v98, 7, s32
	v_add_u32_e32 v38, v38, v39
	v_lshlrev_b32_e32 v35, 4, v35
	s_mov_b32 s35, 0x1869f
	v_mov_b32_e32 v2, 0
	v_mov_b32_e32 v3, 0
	v_mov_b32_e32 v4, 0
	v_mov_b32_e32 v5, 0
	v_mov_b32_e32 v6, 0
	v_mov_b32_e32 v7, 0
	v_mov_b32_e32 v8, 0
	v_mov_b32_e32 v9, 0
	v_mov_b32_e32 v10, 0
	v_mov_b32_e32 v11, 0
	v_mov_b32_e32 v12, 0
	v_mov_b32_e32 v13, 0
	v_mov_b32_e32 v14, 0
	v_mov_b32_e32 v15, 0
	v_mov_b32_e32 v16, 0
	v_mov_b32_e32 v17, 0
	v_mov_b32_e32 v18, 0
	v_mov_b32_e32 v19, 0
	v_mov_b32_e32 v20, 0
	v_mov_b32_e32 v21, 0
	v_mov_b32_e32 v22, 0
	v_mov_b32_e32 v23, 0
	v_mov_b32_e32 v24, 0
	v_mov_b32_e32 v25, 0
	v_mov_b32_e32 v26, 0
	v_mov_b32_e32 v27, 0
	v_mov_b32_e32 v28, 0
	v_mov_b32_e32 v29, 0
	v_mov_b32_e32 v30, 0
	v_mov_b32_e32 v31, 0
	v_mov_b32_e32 v32, 0
	v_mov_b32_e32 v33, 0
	s_waitcnt vmcnt(0) lgkmcnt(0)
	v_mov_b32_e32 v42, v70
	v_mov_b32_e32 v43, v71
	v_mov_b32_e32 v44, v72
	v_mov_b32_e32 v45, v73
	v_mov_b32_e32 v46, v74
	v_mov_b32_e32 v47, v75
	v_mov_b32_e32 v48, v76
	v_mov_b32_e32 v49, v77
	v_mov_b32_e32 v50, v78
	v_mov_b32_e32 v51, v79
	v_mov_b32_e32 v52, v80
	v_mov_b32_e32 v53, v81
	v_lshlrev_b32_e32 v39, 2, v90
	global_load_dword v40, v39, s[30:31]
	global_load_dword v41, v39, s[30:31] offset:4
	s_lshl_b32 s34, s20, 2
	v_min_u32_e32 v42, s35, v42
	v_min_u32_e32 v46, s35, v46
	v_min_u32_e32 v43, s35, v43
	v_min_u32_e32 v47, s35, v47
	v_min_u32_e32 v44, s35, v44
	v_min_u32_e32 v48, s35, v48
	v_min_u32_e32 v45, s35, v45
	v_min_u32_e32 v49, s35, v49
	v_lshl_or_b32 v42, v42, 7, v34
	v_lshl_or_b32 v46, v46, 7, v34
	v_lshl_or_b32 v43, v43, 7, v34
	v_lshl_or_b32 v47, v47, 7, v34
	v_lshl_or_b32 v44, v44, 7, v34
	v_lshl_or_b32 v48, v48, 7, v34
	v_lshl_or_b32 v45, v45, 7, v34
	v_lshl_or_b32 v49, v49, 7, v34
	global_load_dwordx4 v[70:73], v42, s[24:25]
	global_load_dwordx4 v[74:77], v43, s[24:25]
	global_load_dwordx4 v[78:81], v44, s[24:25]
	global_load_dwordx4 v[82:85], v45, s[24:25]
	global_load_dwordx4 v[86:89], v46, s[10:11]
	global_load_dwordx4 v[90:93], v47, s[10:11]
	global_load_dwordx4 v[94:97], v48, s[10:11]
	global_load_dwordx4 v[102:105], v49, s[10:11]
	s_add_i32 s34, s34, 0x80
	v_add_u32_e32 v39, s34, v35
	global_load_dwordx4 v[42:45], v39, s[4:5]
	global_load_dwordx4 v[46:49], v39, s[6:7]
	v_lshlrev_b32_e32 v39, 1, v34
	ds_read_b128 v[112:115], v39 offset:53248
	ds_read_b128 v[116:119], v39 offset:53760
	ds_read_b128 v[120:123], v39 offset:53504

.Lcu_last1:
	v_add_u32_e32 v39, s14, v98
	v_lshlrev_b32_e32 v39, 7, v39
	v_lshl_add_u32 v39, v100, 1, v39
	global_load_dwordx4 v[70:73], v39, s[48:49] offset:48
	global_load_dwordx4 v[74:77], v39, s[48:49] offset:32
	global_load_dwordx4 v[78:81], v39, s[48:49] offset:16
	global_load_dwordx4 v[82:85], v39, s[48:49]

.Lcu_skip2:
	s_nop 9
	v_fma_f32 v110, v67, v112, v69
	v_fma_f32 v111, v67, v113, v69
	v_max_f32_e32 v110, 0, v110
	v_max_f32_e32 v111, 0, v111
	v_cvt_pk_bf16_f32 v106, v110, v111
	v_fma_f32 v110, v67, v114, v69
	v_fma_f32 v111, v67, v115, v69
	v_max_f32_e32 v110, 0, v110
	v_max_f32_e32 v111, 0, v111
	v_cvt_pk_bf16_f32 v107, v110, v111
	v_fma_f32 v110, v67, v116, v69
	v_fma_f32 v111, v67, v117, v69
	v_max_f32_e32 v110, 0, v110
	v_max_f32_e32 v111, 0, v111
	v_cvt_pk_bf16_f32 v108, v110, v111
	v_fma_f32 v110, v67, v118, v69
	v_fma_f32 v111, v67, v119, v69
	v_max_f32_e32 v110, 0, v110
	v_max_f32_e32 v111, 0, v111
	v_cvt_pk_bf16_f32 v109, v110, v111
	s_nop 1
	v_mfma_f32_32x32x16_bf16 v[2:17], v[106:109], v[54:57], v[2:17]
	v_fma_f32 v110, v67, v120, v69
	v_fma_f32 v111, v67, v121, v69
	v_max_f32_e32 v110, 0, v110
	v_max_f32_e32 v111, 0, v111
	v_cvt_pk_bf16_f32 v106, v110, v111
	v_fma_f32 v110, v67, v122, v69
	v_fma_f32 v111, v67, v123, v69
	v_max_f32_e32 v110, 0, v110
	v_max_f32_e32 v111, 0, v111
	v_cvt_pk_bf16_f32 v107, v110, v111
	v_fma_f32 v110, v67, v124, v69
	v_fma_f32 v111, v67, v125, v69
	v_max_f32_e32 v110, 0, v110
	v_max_f32_e32 v111, 0, v111
	v_cvt_pk_bf16_f32 v108, v110, v111
	v_fma_f32 v110, v67, v126, v69
	v_fma_f32 v111, v67, v127, v69
	v_max_f32_e32 v110, 0, v110
	v_max_f32_e32 v111, 0, v111
	v_cvt_pk_bf16_f32 v109, v110, v111
	s_nop 1
	v_mfma_f32_32x32x16_bf16 v[2:17], v[106:109], v[58:61], v[2:17]
	v_lshlrev_b32_e32 v39, 1, v34
	ds_read_b128 v[112:115], v39 offset:53248
	ds_read_b128 v[116:119], v39 offset:53760
	ds_read_b128 v[120:123], v39 offset:53504
	s_add_i32 s20, s20, 32
	s_add_i32 s15, s15, -1
	s_cmp_lg_u32 s15, 0
	s_cbranch_scc1 .Lcu_loop
	s_waitcnt vmcnt(0)
	v_mov_b32_e32 v68, v70
	v_mov_b32_e32 v69, v71
	v_mov_b32_e32 v70, v72
	v_mov_b32_e32 v71, v73
	v_mov_b32_e32 v72, v74
	v_mov_b32_e32 v73, v75
	v_mov_b32_e32 v74, v76
	v_mov_b32_e32 v75, v77
	v_mov_b32_e32 v76, v78
	v_mov_b32_e32 v77, v79
	v_mov_b32_e32 v78, v80
	v_mov_b32_e32 v79, v81
	v_mov_b32_e32 v80, v82
	v_mov_b32_e32 v81, v83
	v_mov_b32_e32 v82, v84
	v_mov_b32_e32 v83, v85
	s_mov_b32 s37, 1
	v_add_u32_e32 v90, s14, v98
	s_branch .LBB8_8

.Lcu_hskip:
	v_cvt_pk_f16_f32 v18, v18, v19
	v_cvt_pk_f16_f32 v19, v20, v21
	v_cvt_pk_f16_f32 v20, v22, v23
	v_cvt_pk_f16_f32 v21, v24, v25
	v_cvt_pk_f16_f32 v2, v2, v3
	v_cvt_pk_f16_f32 v3, v4, v5
	v_cvt_pk_f16_f32 v4, v6, v7
	v_cvt_pk_f16_f32 v5, v8, v9
	v_lshlrev_b32_e32 v66, 2, v98
	s_waitcnt vmcnt(0)
	ds_read_b128 v[46:49], v99 offset:16384
	ds_read_b128 v[84:87], v99 offset:17408
	v_mov_b32_e32 v50, v34
	v_mov_b32_e32 v51, v34
	v_mov_b32_e32 v52, v34
	v_mov_b32_e32 v53, v34
	v_mov_b32_e32 v54, v34
	v_mov_b32_e32 v55, v34
	v_mov_b32_e32 v56, v34
	v_mov_b32_e32 v57, v34
	v_mov_b32_e32 v58, v34
	v_mov_b32_e32 v59, v34
	v_mov_b32_e32 v60, v34
	v_mov_b32_e32 v61, v34
	v_mov_b32_e32 v62, v34
	v_mov_b32_e32 v63, v34
	v_mov_b32_e32 v64, v34
	v_mov_b32_e32 v65, v34
	ds_read_b128 v[88:91], v99 offset:20480
	ds_read_b128 v[92:95], v99 offset:21504
	s_waitcnt lgkmcnt(3)
	v_mfma_f32_32x32x16_f16 v[50:65], v[80:83], v[46:49], v[50:65]
	v_mov_b32_e32 v34, v35
	v_mov_b32_e32 v36, v35
	v_mov_b32_e32 v37, v35
	v_mov_b32_e32 v38, v35
	v_mov_b32_e32 v39, v35
	v_mov_b32_e32 v40, v35
	v_mov_b32_e32 v41, v35
	v_mov_b32_e32 v42, v35
	v_mov_b32_e32 v43, v35
	v_mov_b32_e32 v44, v35
	v_mov_b32_e32 v45, v35
	v_mov_b32_e32 v46, v35
	v_mov_b32_e32 v47, v35
	v_mov_b32_e32 v48, v35
	v_mov_b32_e32 v49, v35
	s_waitcnt lgkmcnt(1)
	s_nop 0
	v_mfma_f32_32x32x16_f16 v[34:49], v[80:83], v[88:91], v[34:49]
	ds_read_b128 v[88:91], v99 offset:24576
	ds_read_b128 v[100:103], v99 offset:25600
	s_waitcnt lgkmcnt(1)
	v_mfma_f32_32x32x16_f16 v[50:65], v[80:83], v[88:91], v[50:65]
	ds_read_b128 v[88:91], v99 offset:28672
	ds_read_b128 v[104:107], v99 offset:29696
	s_waitcnt lgkmcnt(1)
	v_mfma_f32_32x32x16_f16 v[34:49], v[80:83], v[88:91], v[34:49]
	v_mfma_f32_32x32x16_f16 v[50:65], v[76:79], v[84:87], v[50:65]
	v_mfma_f32_32x32x16_f16 v[34:49], v[76:79], v[92:95], v[34:49]
	v_mfma_f32_32x32x16_f16 v[50:65], v[76:79], v[100:103], v[50:65]
	s_waitcnt lgkmcnt(0)
	v_mfma_f32_32x32x16_f16 v[34:49], v[76:79], v[104:107], v[34:49]
	ds_read_b128 v[76:79], v99 offset:18432
	ds_read_b128 v[80:83], v99 offset:19456
	s_waitcnt lgkmcnt(1)
	v_mfma_f32_32x32x16_f16 v[50:65], v[72:75], v[76:79], v[50:65]
	ds_read_b128 v[76:79], v99 offset:22528
	ds_read_b128 v[84:87], v99 offset:23552
	s_waitcnt lgkmcnt(1)
	v_mfma_f32_32x32x16_f16 v[34:49], v[72:75], v[76:79], v[34:49]
	ds_read_b128 v[76:79], v99 offset:26624
	ds_read_b128 v[88:91], v99 offset:27648
	s_waitcnt lgkmcnt(1)
	v_mfma_f32_32x32x16_f16 v[50:65], v[72:75], v[76:79], v[50:65]
	ds_read_b128 v[76:79], v99 offset:30720
	ds_read_b128 v[92:95], v99 offset:31744
	s_waitcnt lgkmcnt(1)
	v_mfma_f32_32x32x16_f16 v[34:49], v[72:75], v[76:79], v[34:49]
	v_mfma_f32_32x32x16_f16 v[50:65], v[68:71], v[80:83], v[50:65]
	v_mfma_f32_32x32x16_f16 v[34:49], v[68:71], v[84:87], v[34:49]
	v_mfma_f32_32x32x16_f16 v[50:65], v[68:71], v[88:91], v[50:65]
	s_waitcnt lgkmcnt(0)
	v_mfma_f32_32x32x16_f16 v[34:49], v[68:71], v[92:95], v[34:49]
	ds_read_b128 v[22:25], v99 offset:32768
	ds_read_b128 v[68:71], v99 offset:33792
	s_waitcnt lgkmcnt(1)
	v_mfma_f32_32x32x16_f16 v[50:65], v[18:21], v[22:25], v[50:65]
	s_waitcnt lgkmcnt(0)
	v_mfma_f32_32x32x16_f16 v[34:49], v[18:21], v[68:71], v[34:49]
	ds_read_b128 v[22:25], v99 offset:40960
	ds_read_b128 v[68:71], v99 offset:41984
	s_waitcnt lgkmcnt(1)
	v_mfma_f32_32x32x16_f16 v[50:65], v[18:21], v[22:25], v[50:65]
	v_cvt_pk_f16_f32 v22, v26, v27
	v_cvt_pk_f16_f32 v23, v28, v29
	v_cvt_pk_f16_f32 v24, v30, v31
	v_cvt_pk_f16_f32 v25, v32, v33
	s_waitcnt lgkmcnt(0)
	v_mfma_f32_32x32x16_f16 v[34:49], v[18:21], v[68:71], v[34:49]
	ds_read_b128 v[18:21], v99 offset:34816
	ds_read_b128 v[26:29], v99 offset:35840
	s_waitcnt lgkmcnt(1)
	v_mfma_f32_32x32x16_f16 v[50:65], v[22:25], v[18:21], v[50:65]
	s_waitcnt lgkmcnt(0)
	v_mfma_f32_32x32x16_f16 v[34:49], v[22:25], v[26:29], v[34:49]
	ds_read_b128 v[18:21], v99 offset:43008
	ds_read_b128 v[26:29], v99 offset:44032
	s_waitcnt lgkmcnt(1)
	v_mfma_f32_32x32x16_f16 v[50:65], v[22:25], v[18:21], v[50:65]
	ds_read_b128 v[6:9], v99 offset:36864
	ds_read_b128 v[18:21], v99 offset:37888
	s_waitcnt lgkmcnt(2)
	v_mfma_f32_32x32x16_f16 v[34:49], v[22:25], v[26:29], v[34:49]
	s_waitcnt lgkmcnt(1)
	v_mfma_f32_32x32x16_f16 v[50:65], v[2:5], v[6:9], v[50:65]
	s_waitcnt lgkmcnt(0)
	v_mfma_f32_32x32x16_f16 v[34:49], v[2:5], v[18:21], v[34:49]
	ds_read_b128 v[6:9], v99 offset:45056
	ds_read_b128 v[18:21], v99 offset:46080
	s_waitcnt lgkmcnt(1)
	v_mfma_f32_32x32x16_f16 v[50:65], v[2:5], v[6:9], v[50:65]
	v_cvt_pk_f16_f32 v8, v10, v11
	v_cvt_pk_f16_f32 v9, v12, v13
	v_cvt_pk_f16_f32 v10, v14, v15
	v_cvt_pk_f16_f32 v11, v16, v17
	s_waitcnt lgkmcnt(0)
	v_mfma_f32_32x32x16_f16 v[34:49], v[2:5], v[18:21], v[34:49]
	ds_read_b128 v[2:5], v99 offset:38912
	ds_read_b128 v[12:15], v99 offset:39936
	s_waitcnt lgkmcnt(1)
	v_mfma_f32_32x32x16_f16 v[50:65], v[8:11], v[2:5], v[50:65]
	s_waitcnt lgkmcnt(0)
	v_mfma_f32_32x32x16_f16 v[34:49], v[8:11], v[12:15], v[34:49]
	ds_read_b128 v[2:5], v99 offset:47104
	ds_read_b128 v[12:15], v99 offset:48128
	s_waitcnt lgkmcnt(1)
	v_mfma_f32_32x32x16_f16 v[50:65], v[8:11], v[2:5], v[50:65]
	v_lshrrev_b32_e32 v2, 3, v0
	v_and_b32_e32 v6, 4, v2
	v_add_u32_e32 v6, s14, v6
	v_ashrrev_i32_e32 v7, 31, v6
	v_lshl_add_u64 v[4:5], s[4:5], 0, v[66:67]
	v_add_u32_e32 v16, 16, v6
	v_ashrrev_i32_e32 v17, 31, v16
	v_lshlrev_b64 v[16:17], 7, v[16:17]
	s_waitcnt lgkmcnt(0)
	v_mfma_f32_32x32x16_f16 v[34:49], v[8:11], v[12:15], v[34:49]
	v_lshlrev_b64 v[8:9], 7, v[6:7]
	v_lshl_add_u64 v[8:9], v[4:5], 0, v[8:9]
	v_add_u32_e32 v12, 8, v6
	v_ashrrev_i32_e32 v13, 31, v12
	v_lshlrev_b64 v[12:13], 7, v[12:13]
	v_lshl_add_u64 v[12:13], v[4:5], 0, v[12:13]
	v_add_u32_e32 v14, 10, v6
	s_nop 4
	v_cvt_pk_bf16_f32 v10, v50, v34
	global_store_dword v[8:9], v10, off
	v_add_u32_e32 v8, 1, v6
	v_ashrrev_i32_e32 v9, 31, v8
	v_add_u32_e32 v10, 2, v6
	v_lshlrev_b64 v[8:9], 7, v[8:9]
	v_ashrrev_i32_e32 v11, 31, v10
	v_cvt_pk_bf16_f32 v7, v51, v35
	v_lshl_add_u64 v[8:9], v[4:5], 0, v[8:9]
	v_lshlrev_b64 v[10:11], 7, v[10:11]
	global_store_dword v[8:9], v7, off
	v_cvt_pk_bf16_f32 v7, v52, v36
	v_lshl_add_u64 v[10:11], v[4:5], 0, v[10:11]
	global_store_dword v[10:11], v7, off
	v_add_u32_e32 v10, 3, v6
	v_ashrrev_i32_e32 v11, 31, v10
	v_lshlrev_b64 v[10:11], 7, v[10:11]
	v_cvt_pk_bf16_f32 v7, v53, v37
	v_lshl_add_u64 v[10:11], v[4:5], 0, v[10:11]
	global_store_dword v[10:11], v7, off
	v_cvt_pk_bf16_f32 v7, v54, v38
	global_store_dword v[12:13], v7, off
	v_add_u32_e32 v12, 9, v6
	v_ashrrev_i32_e32 v13, 31, v12
	v_lshlrev_b64 v[12:13], 7, v[12:13]
	v_ashrrev_i32_e32 v15, 31, v14
	v_cvt_pk_bf16_f32 v7, v55, v39
	v_lshl_add_u64 v[12:13], v[4:5], 0, v[12:13]
	v_lshlrev_b64 v[14:15], 7, v[14:15]
	global_store_dword v[12:13], v7, off
	v_cvt_pk_bf16_f32 v7, v56, v40
	v_lshl_add_u64 v[14:15], v[4:5], 0, v[14:15]
	global_store_dword v[14:15], v7, off
	v_add_u32_e32 v14, 11, v6
	v_ashrrev_i32_e32 v15, 31, v14
	v_lshlrev_b64 v[14:15], 7, v[14:15]
	v_cvt_pk_bf16_f32 v7, v57, v41
	v_lshl_add_u64 v[14:15], v[4:5], 0, v[14:15]
	global_store_dword v[14:15], v7, off
	v_cvt_pk_bf16_f32 v7, v58, v42
	v_lshl_add_u64 v[16:17], v[4:5], 0, v[16:17]
	global_store_dword v[16:17], v7, off
	v_add_u32_e32 v16, 17, v6
	v_ashrrev_i32_e32 v17, 31, v16
	v_add_u32_e32 v18, 18, v6
	v_lshlrev_b64 v[16:17], 7, v[16:17]
	v_ashrrev_i32_e32 v19, 31, v18
	v_cvt_pk_bf16_f32 v7, v59, v43
	v_lshl_add_u64 v[16:17], v[4:5], 0, v[16:17]
	v_lshlrev_b64 v[18:19], 7, v[18:19]
	global_store_dword v[16:17], v7, off
	v_cvt_pk_bf16_f32 v7, v60, v44
	v_lshl_add_u64 v[18:19], v[4:5], 0, v[18:19]
	global_store_dword v[18:19], v7, off
	v_add_u32_e32 v18, 19, v6
	v_ashrrev_i32_e32 v19, 31, v18
	v_add_u32_e32 v20, 24, v6
	v_lshlrev_b64 v[18:19], 7, v[18:19]
	v_ashrrev_i32_e32 v21, 31, v20
	v_cvt_pk_bf16_f32 v7, v61, v45
	v_lshl_add_u64 v[18:19], v[4:5], 0, v[18:19]
	v_lshlrev_b64 v[20:21], 7, v[20:21]
	global_store_dword v[18:19], v7, off
	v_cvt_pk_bf16_f32 v7, v62, v46
	v_lshl_add_u64 v[20:21], v[4:5], 0, v[20:21]
	s_mov_b64 exec, 0xffffffff
	global_store_dword v[20:21], v7, off
	s_mov_b64 exec, -1
	v_add_u32_e32 v20, 25, v6
	v_ashrrev_i32_e32 v21, 31, v20
	v_add_u32_e32 v22, 26, v6
	v_lshlrev_b64 v[20:21], 7, v[20:21]
	v_ashrrev_i32_e32 v23, 31, v22
	v_cvt_pk_bf16_f32 v7, v63, v47
	v_lshl_add_u64 v[20:21], v[4:5], 0, v[20:21]
	v_lshlrev_b64 v[22:23], 7, v[22:23]
	v_cvt_pk_bf16_f32 v7, v64, v48
	v_lshl_add_u64 v[22:23], v[4:5], 0, v[22:23]
	v_add_u32_e32 v6, 27, v6
	v_ashrrev_i32_e32 v7, 31, v6
	v_lshlrev_b64 v[6:7], 7, v[6:7]
	v_mov_b32_e32 v2, v50
	v_mov_b32_e32 v3, v34
	v_cvt_pk_bf16_f32 v22, v65, v49
	v_lshl_add_u64 v[4:5], v[4:5], 0, v[6:7]
	v_mov_b32_e32 v34, v51
	v_mov_b32_e32 v63, 0
	v_mov_b32_e32 v64, 0
	v_mov_b32_e32 v65, 0
	v_mov_b32_e32 v47, 0
	v_mov_b32_e32 v48, 0
	v_mov_b32_e32 v49, 0
	s_mov_b32 exec_lo, 0
	v_mov_b32_e32 v62, 0
	v_mov_b32_e32 v46, 0
	s_mov_b64 exec, -1
	v_pk_add_f32 v[4:5], v[2:3], 0 op_sel_hi:[1,0]
	v_pk_fma_f32 v[2:3], v[2:3], v[2:3], 0 op_sel_hi:[1,1,0]
	v_mov_b32_e32 v8, v52
	v_mov_b32_e32 v9, v36
	v_pk_add_f32 v[4:5], v[4:5], v[34:35]
	v_pk_fma_f32 v[2:3], v[34:35], v[34:35], v[2:3]
	v_mov_b32_e32 v36, v53
	v_pk_add_f32 v[4:5], v[4:5], v[8:9]
	v_pk_fma_f32 v[2:3], v[8:9], v[8:9], v[2:3]
	v_mov_b32_e32 v10, v54
	v_mov_b32_e32 v11, v38
	v_pk_add_f32 v[4:5], v[4:5], v[36:37]
	v_pk_fma_f32 v[2:3], v[36:37], v[36:37], v[2:3]
	v_mov_b32_e32 v38, v55
	v_pk_add_f32 v[4:5], v[4:5], v[10:11]
	v_pk_fma_f32 v[2:3], v[10:11], v[10:11], v[2:3]
	v_mov_b32_e32 v12, v56
	v_mov_b32_e32 v13, v40
	v_pk_add_f32 v[4:5], v[4:5], v[38:39]
	v_pk_fma_f32 v[2:3], v[38:39], v[38:39], v[2:3]
	v_mov_b32_e32 v40, v57
	v_pk_add_f32 v[4:5], v[4:5], v[12:13]
	v_pk_fma_f32 v[2:3], v[12:13], v[12:13], v[2:3]
	v_mov_b32_e32 v14, v58
	v_mov_b32_e32 v15, v42
	v_pk_add_f32 v[4:5], v[4:5], v[40:41]
	v_pk_fma_f32 v[2:3], v[40:41], v[40:41], v[2:3]
	v_mov_b32_e32 v42, v59
	v_pk_add_f32 v[4:5], v[4:5], v[14:15]
	v_pk_fma_f32 v[2:3], v[14:15], v[14:15], v[2:3]
	v_mov_b32_e32 v16, v60
	v_mov_b32_e32 v17, v44
	v_pk_add_f32 v[4:5], v[4:5], v[42:43]
	v_pk_fma_f32 v[2:3], v[42:43], v[42:43], v[2:3]
	v_mov_b32_e32 v44, v61
	v_pk_add_f32 v[4:5], v[4:5], v[16:17]
	v_pk_fma_f32 v[2:3], v[16:17], v[16:17], v[2:3]
	v_mov_b32_e32 v18, v62
	v_mov_b32_e32 v19, v46
	v_pk_add_f32 v[4:5], v[4:5], v[44:45]
	v_pk_fma_f32 v[2:3], v[44:45], v[44:45], v[2:3]
	v_mov_b32_e32 v46, v63
	v_pk_add_f32 v[4:5], v[4:5], v[18:19]
	v_pk_fma_f32 v[2:3], v[18:19], v[18:19], v[2:3]
	v_mov_b32_e32 v20, v64
	v_mov_b32_e32 v21, v48
	v_pk_add_f32 v[4:5], v[4:5], v[46:47]
	v_pk_fma_f32 v[2:3], v[46:47], v[46:47], v[2:3]
	v_mov_b32_e32 v48, v65
	v_pk_add_f32 v[4:5], v[4:5], v[20:21]
	v_pk_fma_f32 v[2:3], v[20:21], v[20:21], v[2:3]
	v_pk_add_f32 v[34:35], v[4:5], v[48:49]
	v_pk_fma_f32 v[36:37], v[48:49], v[48:49], v[2:3]
